# priority scheme: one static s_setprio 1 for waves 4-7 from the input projection on, all 112 per-MFMA-block s_setprio 1/0 toggles in the GEMM K-loops replaced by s_nop 0
# baseline (speedup 1.0000x reference)
;     template <class Tp> __device__ __forceinline__ Tp* W(size_t off) const { return (Tp*)(ws + off); }
;     template <class Tp> __device__ __forceinline__ const Tp* I(int k) const { return (const Tp*)a->in[k]; }
;     __device__ __forceinline__ bool next(int i, Unit& u) const {
;         int L = i * G + c;
;         if (G == 256) {
;             if (i == 8) { if (c >= 176) return false; L = 2048 + c; }
;             else if (i == 9) { if (c >= 80) return false; L = 2224 + c; }
;             else if (i > 9) return false;
;         }
;         if (L >= 64 * NT8) return false;
;         int pm, pn; pg8::tile_of(L, 64, NT8, pm, pn); if (pn >= TL_P) pn += TL_G - TL_P; u.pm = pm; u.pn = pn; u.a = xb8 + (size_t)pm * 256 * DM; u.b = wint + (size_t)pn * 256 * DM * 2;
;         u.kind = pn < TL_P ? KD_A : pn < TL_Q ? KD_G : pn < TL_K ? KD_Q : pn < TL_V ? KD_K : KD_V; u.aux = 0; return true;
; __global__ void __launch_bounds__(512, 2) fwd_kernel(Args args) {
;     ...
;     if (IN(1)) {
;         SchedG1F S8{F.G, F.bid, F.W<char>(WS_XB8), F.W<char>(WS_WINT)};
;         SchedG1 S{F.G, F.G - 1 - F.bid, F.W<char>(WS_XB), F.W<char>(WS_WINT), F.W<char>(WS_MEMB), F.W<char>(WS_WKVT)};
;         EpiG1 E{F.W<float>(WS_RS0), F.W<float>(WS_RSMEM), F.W<float>(WS_ROPEQK), F.W<float>(WS_ROPEI), F.W<bf16_t>(WS_ABUF), F.W<bf16_t>(WS_PBUF), F.W<bf16_t>(WS_GABUF),
;                 F.W<bf16_t>(WS_QB), F.W<bf16_t>(WS_KB), F.W<bf16_t>(WS_VB), F.W<bf16_t>(WS_QIB), F.W<bf16_t>(WS_KIB), F.W<float>(WS_WIB), F.W<bf16_t>(WS_KX), F.W<bf16_t>(WS_VX), 1.0f / W8_SCALE};
;         pg8::SideConv SD{F.I<float>(IN_W_GU), F.W<unsigned char>(WS_WGUT), 1, 0, SJ_GU_P1, F.G, F.bid};
;         const int sdone8 = pg8::gemm_phase<EpiG1, SchedG1F, pg8::SideConv, true>(F.lds, DM, S8, E, F.wave, SD);
.LBB0_557:
	s_cmp_lt_i32 s26, 2
	s_cselect_b64 s[0:1], -1, 0
	s_cmp_gt_i32 s27, 1
	s_cselect_b64 s[2:3], -1, 0
	s_and_b64 s[0:1], s[0:1], s[2:3]
	s_andn2_b64 vcc, exec, s[0:1]
	s_cbranch_vccnz .LBB0_1455
	s_cmp_lt_u32 s93, 4
	s_cbranch_scc1 .Lp1prio
	s_setprio 1
.Lp1prio:
	s_add_u32 s11, s24, 0xa5f09800
	s_addc_u32 s14, s25, 0
	s_add_u32 s8, s24, 0x4729000
	s_addc_u32 s9, s25, 0
	s_cmpk_lt_i32 s18, 0x900
	s_cselect_b64 s[0:1], -1, 0
	s_cmpk_gt_i32 s18, 0x8ff
	v_mbcnt_lo_u32_b32 v8, -1, 0
	v_mbcnt_hi_u32_b32 v8, -1, v8
	s_cbranch_scc1 .LBB0_560
	s_ashr_i32 s2, s18, 31
	s_lshr_b32 s2, s2, 29
	s_add_i32 s2, s18, s2
	s_and_b32 s3, s2, -8
	s_sub_i32 s3, s18, s3
	s_cmp_lt_i32 s3, 0
	s_movk_i32 s4, 0x121
	s_cselect_b32 s4, s4, 0x120
	s_mul_i32 s3, s4, s3
	s_ashr_i32 s2, s2, 3
	s_add_i32 s3, s3, s2
	s_mul_hi_i32 s2, s3, 0x38e38e39
	s_lshr_b32 s4, s2, 31
	s_ashr_i32 s2, s2, 6
	s_add_i32 s2, s2, s4
	s_lshl_b32 s4, s2, 3
	s_mulk_i32 s2, 0x120
	s_sub_i32 s2, s3, s2
	s_sext_i32_i16 s3, s2
	s_bfe_u32 s3, s3, 0x3001c
	s_add_i32 s3, s2, s3
	s_sext_i32_i16 s5, s3
	s_and_b32 s3, s3, 0xfff8
	s_sub_i32 s3, s2, s3
	s_sext_i32_i16 s3, s3
	s_add_i32 s16, s4, s3
	s_ashr_i32 s3, s5, 3
	s_add_i32 s4, s3, 16
	s_cmpk_gt_i32 s2, 0x7f
	s_cselect_b32 s4, s4, s3
	s_ashr_i32 s17, s16, 31
	s_lshl_b64 s[2:3], s[16:17], 19
	s_add_u32 s2, s11, s2
	s_addc_u32 s3, s14, s3
	s_ashr_i32 s5, s4, 31
	s_lshl_b64 s[6:7], s[4:5], 20
	s_add_u32 s76, s8, s6
	s_addc_u32 s77, s9, s7
	s_cmp_lt_u32 s4, 50
	s_cselect_b32 s5, 4, 5
	s_cmp_gt_u32 s4, 47
	s_cselect_b32 s5, s5, 3
	s_cmp_gt_u32 s4, 39
	s_cselect_b32 s5, s5, 2
	s_cmp_gt_i32 s4, 15
	s_cselect_b32 s55, s5, 0
	s_branch .LBB0_561

;     template <class Tp> __device__ __forceinline__ Tp* W(size_t off) const { return (Tp*)(ws + off); }
;     template <class Tp> __device__ __forceinline__ const Tp* I(int k) const { return (const Tp*)a->in[k]; }
; #define GRID_BAR() xcd_barrier(bar)
; #define GRID_BAR() do { } while (0)
; #define BOTH(k) (IN(k) && IN((k) + 1))
; __global__ void __launch_bounds__(512, 2) fwd_kernel(Args args) {
;     ...
;     if (IN(2)) { pg8::SideConv SD{F.I<float>(IN_W_GU), F.W<unsigned char>(WS_WGUT), 1, SJ_GU_P1, SJ_GU_P2, F.G, F.bid};
;                  ix::indexer_phase(F, F.W<bf16_t>(WS_QIB), F.W<bf16_t>(WS_KIB), F.W<float>(WS_WIB), F.W<unsigned>(WS_MASK), SD); if (BOTH(2)) GRID_BAR(); }
.LBB0_1455:
	s_cmp_lt_i32 s26, 3
	s_cselect_b64 s[0:1], -1, 0
	s_cmp_gt_i32 s27, 2
	s_cselect_b64 s[2:3], -1, 0
	s_and_b64 s[0:1], s[0:1], s[2:3]
	s_andn2_b64 vcc, exec, s[0:1]
	s_cbranch_vccnz .LBB0_1780
	s_cmp_lt_u32 s93, 4
	s_cbranch_scc1 .Lp2prio
	s_nop 0

;     template <class Tp> __device__ __forceinline__ Tp* W(size_t off) const { return (Tp*)(ws + off); }
;     template <class Tp> __device__ __forceinline__ const Tp* I(int k) const { return (const Tp*)a->in[k]; }
; __global__ void __launch_bounds__(512, 2) fwd_kernel(Args args) {
;     ...
;     if (IN(3)) {
;         att::AttnTensors X{F.W<bf16_t>(WS_QB), F.W<bf16_t>(WS_KB), F.W<bf16_t>(WS_VB), F.W<bf16_t>(WS_YATT), F.W<unsigned>(WS_MASK)};
;         att::MergeArgs MG{F.ws, F.I<float>(IN_CONV_W)};
;         att::attn_phase<DM, 512, DM, true, 6, true>((char*)lds_raw, X, MG, NB, NHEAD, NKVH, SEQ, SEQ, 0, att::ORDER_PAIRED | att::ORDER_XCD, F.G, F.bid, F.wave);
.LBB0_1780:
	s_nop 0
	s_cmp_lt_i32 s26, 4
	s_cselect_b64 s[0:1], -1, 0
	s_cmp_gt_i32 s27, 3
	s_cselect_b64 s[2:3], -1, 0
	s_and_b64 s[0:1], s[0:1], s[2:3]
	s_andn2_b64 vcc, exec, s[0:1]
	s_cbranch_vccnz .LBB0_2032
	s_abs_i32 s0, s19
	v_cvt_f32_u32_e32 v0, s0
	s_add_i32 s1, s19, 0x1ff
	s_sub_i32 s2, 0xfffffe01, s19
	s_xor_b32 s3, s1, s19
	v_rcp_iflag_f32_e32 v0, v0
	s_max_i32 s1, s1, s2
	s_sub_i32 s2, 0, s0
	s_ashr_i32 s3, s3, 31
	v_mul_f32_e32 v0, 0x4f7ffffe, v0
	v_cvt_u32_f32_e32 v0, v0
	s_mov_b32 s95, 0
	v_readfirstlane_b32 s4, v0
	s_mul_i32 s2, s2, s4
	s_mul_hi_u32 s2, s4, s2
	s_add_i32 s4, s4, s2
	s_mul_hi_u32 s2, s1, s4
	s_mul_i32 s4, s2, s0
	s_sub_i32 s1, s1, s4
	s_add_i32 s5, s2, 1
	s_sub_i32 s4, s1, s0
	s_cmp_ge_u32 s1, s0
	s_cselect_b32 s2, s5, s2
	s_cselect_b32 s1, s4, s1
	s_add_i32 s4, s2, 1
	s_cmp_ge_u32 s1, s0
	s_cselect_b32 s0, s4, s2
	s_xor_b32 s0, s0, s3
	s_sub_i32 s11, s0, s3
	s_cmp_lt_i32 s11, 1
	s_cbranch_scc1 .LBB0_1975
	s_lshl_b32 s7, s18, 2
	s_lshl_b32 s5, s19, 2
	s_mov_b32 s6, 0
	s_mov_b32 s8, s18
	s_branch .LBB0_1784
